# sgu epilogue: the four u loads of each row group issued together (2 exposed load latencies per item instead of 8)
# baseline (speedup 1.0000x reference)
.LBB0_1006:
	ds_read_b64_tr_b16 v[82:83], v154
	ds_read_b64_tr_b16 v[86:87], v154 offset:32
	ds_read_b64_tr_b16 v[84:85], v145 offset:576
	ds_read_b64_tr_b16 v[88:89], v145 offset:608
	ds_read_b64_tr_b16 v[90:91], v154 offset:64
	ds_read_b64_tr_b16 v[92:93], v145 offset:640
	ds_read_b64_tr_b16 v[94:95], v154 offset:96
	ds_read_b64_tr_b16 v[96:97], v145 offset:672
	ds_read_b128 v[98:101], v155 offset:18432
	ds_read_b128 v[134:137], v155 offset:22784
	s_add_i32 s2, s22, s14
	s_ashr_i32 s3, s2, 31
	s_lshr_b32 s3, s3, 25
	s_waitcnt lgkmcnt(1)
	v_mfma_f32_16x16x32_bf16 v[102:105], v[82:85], v[98:101], 0
	s_add_i32 s3, s2, s3
	s_and_b32 s16, s3, 0xffffff80
	s_sub_i32 s14, s2, s16
	v_mfma_f32_16x16x32_bf16 v[106:109], v[86:89], v[98:101], 0
	s_ashr_i32 s15, s14, 31
	s_lshl_b64 s[14:15], s[14:15], 7
	s_ashr_i32 s17, s3, 7
	v_mfma_f32_16x16x32_bf16 v[110:113], v[90:93], v[98:101], 0
	s_lshl_b32 s18, s17, 6
	s_ashr_i32 s19, s18, 31
	v_mfma_f32_16x16x32_bf16 v[98:101], v[94:97], v[98:101], 0
	s_waitcnt lgkmcnt(0)
	v_mfma_f32_16x16x32_bf16 v[82:85], v[82:85], v[134:137], 0
	v_mfma_f32_16x16x32_bf16 v[86:89], v[86:89], v[134:137], 0
	v_mfma_f32_16x16x32_bf16 v[90:93], v[90:93], v[134:137], 0
	v_mfma_f32_16x16x32_bf16 v[94:97], v[94:97], v[134:137], 0
	ds_read_b64_tr_b16 v[134:135], v154 offset:4608
	ds_read_b64_tr_b16 v[136:137], v145 offset:5184
	ds_read_b64_tr_b16 v[138:139], v154 offset:4640
	ds_read_b64_tr_b16 v[140:141], v145 offset:5216
	ds_read_b64_tr_b16 v[160:161], v154 offset:4672
	ds_read_b64_tr_b16 v[162:163], v145 offset:5248
	ds_read_b64_tr_b16 v[164:165], v154 offset:4704
	ds_read_b64_tr_b16 v[166:167], v145 offset:5280
	ds_read_b128 v[168:171], v155 offset:18496
	s_waitcnt lgkmcnt(0)
	v_mfma_f32_16x16x32_bf16 v[102:105], v[134:137], v[168:171], v[102:105]
	v_mfma_f32_16x16x32_bf16 v[106:109], v[138:141], v[168:171], v[106:109]
	v_mfma_f32_16x16x32_bf16 v[110:113], v[160:163], v[168:171], v[110:113]
	v_mfma_f32_16x16x32_bf16 v[98:101], v[164:167], v[168:171], v[98:101]
	ds_read_b128 v[168:171], v155 offset:22848
	s_waitcnt lgkmcnt(0)
	v_mfma_f32_16x16x32_bf16 v[82:85], v[134:137], v[168:171], v[82:85]
	v_mfma_f32_16x16x32_bf16 v[86:89], v[138:141], v[168:171], v[86:89]
	v_mfma_f32_16x16x32_bf16 v[90:93], v[160:163], v[168:171], v[90:93]
	v_mfma_f32_16x16x32_bf16 v[94:97], v[164:167], v[168:171], v[94:97]
	ds_read_b64_tr_b16 v[134:135], v154 offset:9216
	ds_read_b64_tr_b16 v[136:137], v145 offset:9792
	ds_read_b64_tr_b16 v[138:139], v154 offset:9248
	ds_read_b64_tr_b16 v[140:141], v145 offset:9824
	ds_read_b64_tr_b16 v[160:161], v154 offset:9280
	ds_read_b64_tr_b16 v[162:163], v145 offset:9856
	ds_read_b64_tr_b16 v[164:165], v154 offset:9312
	ds_read_b64_tr_b16 v[166:167], v145 offset:9888
	ds_read_b128 v[168:171], v155 offset:18560
	s_waitcnt lgkmcnt(0)
	v_mfma_f32_16x16x32_bf16 v[172:175], v[160:163], v[168:171], v[110:113]
	s_nop 2
	ds_read_b128 v[110:113], v155 offset:22912
	v_mfma_f32_16x16x32_bf16 v[102:105], v[134:137], v[168:171], v[102:105]
	v_mfma_f32_16x16x32_bf16 v[106:109], v[138:141], v[168:171], v[106:109]
	v_mfma_f32_16x16x32_bf16 v[98:101], v[164:167], v[168:171], v[98:101]
	s_waitcnt lgkmcnt(0)
	v_mfma_f32_16x16x32_bf16 v[82:85], v[134:137], v[110:113], v[82:85]
	v_mfma_f32_16x16x32_bf16 v[86:89], v[138:141], v[110:113], v[86:89]
	v_mfma_f32_16x16x32_bf16 v[134:137], v[160:163], v[110:113], v[90:93]
	v_mfma_f32_16x16x32_bf16 v[138:141], v[164:167], v[110:113], v[94:97]
	s_nop 1
	ds_read_b64_tr_b16 v[90:91], v154 offset:13824
	ds_read_b64_tr_b16 v[92:93], v145 offset:14400
	ds_read_b64_tr_b16 v[160:161], v154 offset:13856
	ds_read_b64_tr_b16 v[162:163], v145 offset:14432
	ds_read_b64_tr_b16 v[164:165], v154 offset:13888
	ds_read_b64_tr_b16 v[166:167], v145 offset:14464
	ds_read_b64_tr_b16 v[168:169], v154 offset:13920
	ds_read_b64_tr_b16 v[170:171], v145 offset:14496
	ds_read_b128 v[94:97], v155 offset:18624
	s_waitcnt lgkmcnt(0)
	v_mfma_f32_16x16x32_bf16 v[110:113], v[90:93], v[94:97], v[102:105]
	v_mfma_f32_16x16x32_bf16 v[102:105], v[164:167], v[94:97], v[172:175]
	s_nop 2
	ds_read_b128 v[172:175], v155 offset:22976
	v_mfma_f32_16x16x32_bf16 v[106:109], v[160:163], v[94:97], v[106:109]
	v_mfma_f32_16x16x32_bf16 v[98:101], v[168:171], v[94:97], v[98:101]
	s_waitcnt lgkmcnt(0)
	v_mfma_f32_16x16x32_bf16 v[94:97], v[90:93], v[172:175], v[82:85]
	v_mfma_f32_16x16x32_bf16 v[90:93], v[160:163], v[172:175], v[86:89]
	v_mfma_f32_16x16x32_bf16 v[86:89], v[164:167], v[172:175], v[134:137]
	v_mfma_f32_16x16x32_bf16 v[82:85], v[168:171], v[172:175], v[138:141]
	s_nop 1
	v_mov_b64_e32 v[136:137], s[0:1]
	v_or_b32_e32 v134, s16, v116
	v_ashrrev_i32_e32 v135, 31, v134
	v_or_b32_e32 v138, s14, v116
	v_mad_u64_u32 v[136:137], s[20:21], v138, s25, v[136:137]
	v_mad_i32_i24 v137, s15, v157, v137
	v_lshl_add_u64 v[136:137], s[18:19], 1, v[136:137]
	v_lshl_add_u64 v[136:137], v[136:137], 0, v[114:115]
	v_add_co_u32_e32 v140, vcc, 0x1000, v136
	v_lshl_add_u64 v[134:135], v[134:135], 2, s[4:5]
	s_nop 0
	v_addc_co_u32_e32 v141, vcc, 0, v137, vcc
	global_load_dwordx2 v[176:177], v[140:141], off offset:4000
	global_load_dwordx2 v[178:179], v[140:141], off offset:4032
	global_load_dwordx2 v[180:181], v[140:141], off offset:4064
	global_load_dwordx2 v[140:141], v[140:141], off offset:3968
	v_mov_b32_e32 v139, s15
	global_load_dword v134, v[134:135], off
	s_waitcnt vmcnt(1)
	v_lshlrev_b32_e32 v123, 16, v140
	v_mul_f32_e32 v125, 0x3d372713, v123
	v_mul_f32_e32 v125, v125, v123
	v_fma_f32 v125, v125, v123, v123
	v_mul_f32_e32 v125, 0x3f4c422a, v125
	v_add_f32_e64 v127, |v125|, |v125|
	v_mul_f32_e32 v127, 0x3fb8aa3b, v127
	v_exp_f32_e32 v127, v127
	s_nop 0
	v_add_f32_e32 v127, 1.0, v127
	v_rcp_f32_e32 v127, v127
	s_nop 0
	v_fma_f32 v127, v127, -2.0, 1.0
	v_and_b32_e32 v129, 0xffff0000, v140
	v_mul_f32_e32 v131, 0x3d372713, v129
	v_mul_f32_e32 v131, v131, v129
	v_fma_f32 v131, v131, v129, v129
	v_mul_f32_e32 v131, 0x3f4c422a, v131
	v_add_f32_e64 v132, |v131|, |v131|
	v_mul_f32_e32 v132, 0x3fb8aa3b, v132
	v_exp_f32_e32 v132, v132
	s_nop 0
	v_add_f32_e32 v132, 1.0, v132
	v_rcp_f32_e32 v132, v132
	s_nop 0
	v_fma_f32 v132, v132, -2.0, 1.0
	v_lshlrev_b32_e32 v135, 16, v141
	v_mul_f32_e32 v140, 0x3d372713, v135
	v_mul_f32_e32 v140, v140, v135
	v_fma_f32 v140, v140, v135, v135
	v_mul_f32_e32 v140, 0x3f4c422a, v140
	v_add_f32_e64 v159, |v140|, |v140|
	v_mul_f32_e32 v159, 0x3fb8aa3b, v159
	v_exp_f32_e32 v159, v159
	s_nop 0
	v_add_f32_e32 v159, 1.0, v159
	v_rcp_f32_e32 v159, v159
	s_nop 0
	v_fma_f32 v159, v159, -2.0, 1.0
	v_and_b32_e32 v141, 0xffff0000, v141
	v_mul_f32_e32 v160, 0x3d372713, v141
	v_mul_f32_e32 v160, v160, v141
	v_fma_f32 v160, v160, v141, v141
	v_mul_f32_e32 v160, 0x3f4c422a, v160
	v_add_f32_e64 v161, |v160|, |v160|
	v_mul_f32_e32 v161, 0x3fb8aa3b, v161
	v_exp_f32_e32 v161, v161
	s_nop 0
	v_add_f32_e32 v161, 1.0, v161
	v_rcp_f32_e32 v161, v161
	s_nop 0
	v_fma_f32 v161, v161, -2.0, 1.0
	v_bfi_b32 v140, s30, v159, v140
	v_mul_f32_e32 v135, 0.5, v135
	v_add_f32_e32 v140, 1.0, v140
	v_mul_f32_e32 v135, v135, v140
	s_waitcnt vmcnt(0)
	v_add_f32_e32 v112, v112, v134
	v_mul_f32_e32 v140, v112, v135
	v_mul_f32_e32 v112, 0.5, v123
	v_bfi_b32 v123, s30, v127, v125
	v_add_f32_e32 v123, 1.0, v123
	v_mul_f32_e32 v112, v112, v123
	v_add_f32_e32 v110, v110, v134
	v_bfi_b32 v135, s30, v132, v131
	v_mov_b32_e32 v132, v111
	v_mul_f32_e32 v112, v110, v112
	v_mul_f32_e32 v123, 0.5, v129
	v_pk_add_f32 v[110:111], v[132:133], v[134:135]
	v_bfi_b32 v135, s30, v161, v160
	v_mul_f32_e32 v111, v123, v111
	v_mul_f32_e32 v110, v110, v111
	v_mov_b32_e32 v132, v113
	v_cvt_pk_bf16_f32 v112, v112, v110
	v_lshlrev_b64 v[110:111], 12, v[138:139]
	v_mul_f32_e32 v123, 0.5, v141
	v_pk_add_f32 v[138:139], v[132:133], v[134:135]
	v_lshl_add_u64 v[110:111], s[8:9], 0, v[110:111]
	v_mul_f32_e32 v113, v123, v139
	v_lshl_add_u64 v[110:111], s[18:19], 1, v[110:111]
	v_mul_f32_e32 v113, v138, v113
	v_lshl_add_u64 v[136:137], v[136:137], 0, s[10:11]
	v_lshl_add_u64 v[110:111], v[110:111], 0, v[114:115]
	v_cvt_pk_bf16_f32 v113, v140, v113
	global_store_dwordx2 v[110:111], v[112:113], off offset:2048
	v_mov_b64_e32 v[112:113], v[176:177]
	v_lshlrev_b32_e32 v123, 16, v112
	v_mul_f32_e32 v125, 0x3d372713, v123
	v_mul_f32_e32 v125, v125, v123
	v_fma_f32 v125, v125, v123, v123
	v_mul_f32_e32 v125, 0x3f4c422a, v125
	v_add_f32_e64 v127, |v125|, |v125|
	v_mul_f32_e32 v127, 0x3fb8aa3b, v127
	v_exp_f32_e32 v127, v127
	s_nop 0
	v_add_f32_e32 v127, 1.0, v127
	v_rcp_f32_e32 v127, v127
	s_nop 0
	v_fma_f32 v127, v127, -2.0, 1.0
	v_and_b32_e32 v112, 0xffff0000, v112
	v_mul_f32_e32 v129, 0x3d372713, v112
	v_mul_f32_e32 v129, v129, v112
	v_fma_f32 v129, v129, v112, v112
	v_mul_f32_e32 v129, 0x3f4c422a, v129
	v_add_f32_e64 v131, |v129|, |v129|
	v_mul_f32_e32 v131, 0x3fb8aa3b, v131
	v_exp_f32_e32 v131, v131
	s_nop 0
	v_add_f32_e32 v131, 1.0, v131
	v_rcp_f32_e32 v131, v131
	s_nop 0
	v_fma_f32 v131, v131, -2.0, 1.0
	v_lshlrev_b32_e32 v132, 16, v113
	v_mul_f32_e32 v135, 0x3d372713, v132
	v_mul_f32_e32 v135, v135, v132
	v_fma_f32 v135, v135, v132, v132
	v_mul_f32_e32 v135, 0x3f4c422a, v135
	v_add_f32_e64 v138, |v135|, |v135|
	v_mul_f32_e32 v138, 0x3fb8aa3b, v138
	v_exp_f32_e32 v138, v138
	s_nop 0
	v_add_f32_e32 v138, 1.0, v138
	v_rcp_f32_e32 v138, v138
	s_nop 0
	v_fma_f32 v138, v138, -2.0, 1.0
	v_and_b32_e32 v113, 0xffff0000, v113
	v_mul_f32_e32 v139, 0x3d372713, v113
	v_mul_f32_e32 v139, v139, v113
	v_fma_f32 v139, v139, v113, v113
	v_mul_f32_e32 v139, 0x3f4c422a, v139
	v_add_f32_e64 v140, |v139|, |v139|
	v_mul_f32_e32 v140, 0x3fb8aa3b, v140
	v_exp_f32_e32 v140, v140
	s_nop 0
	v_add_f32_e32 v140, 1.0, v140
	v_rcp_f32_e32 v140, v140
	s_nop 0
	v_fma_f32 v140, v140, -2.0, 1.0
	v_bfi_b32 v135, s30, v138, v135
	v_mul_f32_e32 v132, 0.5, v132
	v_add_f32_e32 v135, 1.0, v135
	v_mul_f32_e32 v132, v132, v135
	v_add_f32_e32 v108, v108, v134
	v_mul_f32_e32 v138, v108, v132
	v_mul_f32_e32 v108, 0.5, v123
	v_bfi_b32 v123, s30, v127, v125
	v_add_f32_e32 v123, 1.0, v123
	v_mul_f32_e32 v108, v108, v123
	v_add_f32_e32 v106, v106, v134
	v_bfi_b32 v135, s30, v131, v129
	v_mov_b32_e32 v132, v107
	v_mul_f32_e32 v108, v106, v108
	v_mul_f32_e32 v112, 0.5, v112
	v_pk_add_f32 v[106:107], v[132:133], v[134:135]
	v_bfi_b32 v135, s30, v140, v139
	v_mul_f32_e32 v107, v112, v107
	v_mul_f32_e32 v106, v106, v107
	v_mov_b32_e32 v132, v109
	v_cvt_pk_bf16_f32 v106, v108, v106
	v_mul_f32_e32 v107, 0.5, v113
	v_pk_add_f32 v[108:109], v[132:133], v[134:135]
	s_nop 0
	v_mul_f32_e32 v107, v107, v109
	v_mul_f32_e32 v107, v108, v107
	v_cvt_pk_bf16_f32 v107, v138, v107
	global_store_dwordx2 v[110:111], v[106:107], off offset:2080
	v_mov_b64_e32 v[106:107], v[178:179]
	v_lshlrev_b32_e32 v108, 16, v106
	v_mul_f32_e32 v109, 0x3d372713, v108
	v_mul_f32_e32 v109, v109, v108
	v_fma_f32 v109, v109, v108, v108
	v_mul_f32_e32 v109, 0x3f4c422a, v109
	v_add_f32_e64 v112, |v109|, |v109|
	v_mul_f32_e32 v112, 0x3fb8aa3b, v112
	v_exp_f32_e32 v112, v112
	s_nop 0
	v_add_f32_e32 v112, 1.0, v112
	v_rcp_f32_e32 v112, v112
	s_nop 0
	v_fma_f32 v112, v112, -2.0, 1.0
	v_and_b32_e32 v106, 0xffff0000, v106
	v_mul_f32_e32 v113, 0x3d372713, v106
	v_mul_f32_e32 v113, v113, v106
	v_fma_f32 v113, v113, v106, v106
	v_mul_f32_e32 v113, 0x3f4c422a, v113
	v_add_f32_e64 v123, |v113|, |v113|
	v_mul_f32_e32 v123, 0x3fb8aa3b, v123
	v_exp_f32_e32 v123, v123
	s_nop 0
	v_add_f32_e32 v123, 1.0, v123
	v_rcp_f32_e32 v123, v123
	s_nop 0
	v_fma_f32 v123, v123, -2.0, 1.0
	v_lshlrev_b32_e32 v125, 16, v107
	v_mul_f32_e32 v127, 0x3d372713, v125
	v_mul_f32_e32 v127, v127, v125
	v_fma_f32 v127, v127, v125, v125
	v_mul_f32_e32 v127, 0x3f4c422a, v127
	v_add_f32_e64 v129, |v127|, |v127|
	v_mul_f32_e32 v129, 0x3fb8aa3b, v129
	v_exp_f32_e32 v129, v129
	s_nop 0
	v_add_f32_e32 v129, 1.0, v129
	v_rcp_f32_e32 v129, v129
	s_nop 0
	v_fma_f32 v129, v129, -2.0, 1.0
	v_and_b32_e32 v107, 0xffff0000, v107
	v_mul_f32_e32 v131, 0x3d372713, v107
	v_mul_f32_e32 v131, v131, v107
	v_fma_f32 v131, v131, v107, v107
	v_mul_f32_e32 v131, 0x3f4c422a, v131
	v_add_f32_e64 v138, |v131|, |v131|
	v_mul_f32_e32 v138, 0x3fb8aa3b, v138
	v_exp_f32_e32 v138, v138
	s_nop 0
	v_add_f32_e32 v138, 1.0, v138
	v_rcp_f32_e32 v138, v138
	s_nop 0
	v_fma_f32 v138, v138, -2.0, 1.0
	v_bfi_b32 v127, s30, v129, v127
	v_mul_f32_e32 v125, 0.5, v125
	v_add_f32_e32 v127, 1.0, v127
	v_mul_f32_e32 v125, v125, v127
	v_add_f32_e32 v104, v104, v134
	v_mul_f32_e32 v125, v104, v125
	v_mul_f32_e32 v104, 0.5, v108
	v_bfi_b32 v108, s30, v112, v109
	v_add_f32_e32 v108, 1.0, v108
	v_mul_f32_e32 v104, v104, v108
	v_add_f32_e32 v102, v102, v134
	v_bfi_b32 v135, s30, v123, v113
	v_mov_b32_e32 v132, v103
	v_mul_f32_e32 v104, v102, v104
	v_mul_f32_e32 v106, 0.5, v106
	v_pk_add_f32 v[102:103], v[132:133], v[134:135]
	v_bfi_b32 v135, s30, v138, v131
	v_mul_f32_e32 v103, v106, v103
	v_mul_f32_e32 v102, v102, v103
	v_mov_b32_e32 v132, v105
	v_cvt_pk_bf16_f32 v102, v104, v102
	v_mul_f32_e32 v103, 0.5, v107
	v_pk_add_f32 v[104:105], v[132:133], v[134:135]
	s_nop 0
	v_mul_f32_e32 v103, v103, v105
	v_mul_f32_e32 v103, v104, v103
	v_cvt_pk_bf16_f32 v103, v125, v103
	global_store_dwordx2 v[110:111], v[102:103], off offset:2112
	v_mov_b64_e32 v[102:103], v[180:181]
	v_lshlrev_b32_e32 v104, 16, v102
	v_mul_f32_e32 v105, 0x3d372713, v104
	v_mul_f32_e32 v105, v105, v104
	v_fma_f32 v105, v105, v104, v104
	v_mul_f32_e32 v105, 0x3f4c422a, v105
	v_add_f32_e64 v106, |v105|, |v105|
	v_mul_f32_e32 v106, 0x3fb8aa3b, v106
	v_exp_f32_e32 v106, v106
	s_nop 0
	v_add_f32_e32 v106, 1.0, v106
	v_rcp_f32_e32 v106, v106
	s_nop 0
	v_fma_f32 v106, v106, -2.0, 1.0
	v_and_b32_e32 v102, 0xffff0000, v102
	v_mul_f32_e32 v107, 0x3d372713, v102
	v_mul_f32_e32 v107, v107, v102
	v_fma_f32 v107, v107, v102, v102
	v_mul_f32_e32 v107, 0x3f4c422a, v107
	v_add_f32_e64 v108, |v107|, |v107|
	v_mul_f32_e32 v108, 0x3fb8aa3b, v108
	v_exp_f32_e32 v108, v108
	s_nop 0
	v_add_f32_e32 v108, 1.0, v108
	v_rcp_f32_e32 v108, v108
	s_nop 0
	v_fma_f32 v108, v108, -2.0, 1.0
	v_lshlrev_b32_e32 v109, 16, v103
	v_mul_f32_e32 v112, 0x3d372713, v109
	v_mul_f32_e32 v112, v112, v109
	v_fma_f32 v112, v112, v109, v109
	v_mul_f32_e32 v112, 0x3f4c422a, v112
	v_add_f32_e64 v113, |v112|, |v112|
	v_mul_f32_e32 v113, 0x3fb8aa3b, v113
	v_exp_f32_e32 v113, v113
	s_nop 0
	v_add_f32_e32 v113, 1.0, v113
	v_rcp_f32_e32 v113, v113
	s_nop 0
	v_fma_f32 v113, v113, -2.0, 1.0
	v_and_b32_e32 v103, 0xffff0000, v103
	v_mul_f32_e32 v123, 0x3d372713, v103
	v_mul_f32_e32 v123, v123, v103
	v_fma_f32 v123, v123, v103, v103
	v_mul_f32_e32 v123, 0x3f4c422a, v123
	v_add_f32_e64 v125, |v123|, |v123|
	v_mul_f32_e32 v125, 0x3fb8aa3b, v125
	v_exp_f32_e32 v125, v125
	s_nop 0
	v_add_f32_e32 v125, 1.0, v125
	v_rcp_f32_e32 v125, v125
	s_nop 0
	v_fma_f32 v125, v125, -2.0, 1.0
	v_bfi_b32 v112, s30, v113, v112
	v_mul_f32_e32 v109, 0.5, v109
	v_add_f32_e32 v112, 1.0, v112
	v_mul_f32_e32 v109, v109, v112
	v_add_f32_e32 v100, v100, v134
	v_mul_f32_e32 v109, v100, v109
	v_mul_f32_e32 v100, 0.5, v104
	v_bfi_b32 v104, s30, v106, v105
	v_add_f32_e32 v104, 1.0, v104
	v_mul_f32_e32 v100, v100, v104
	v_add_f32_e32 v98, v98, v134
	v_bfi_b32 v135, s30, v108, v107
	v_mov_b32_e32 v132, v99
	v_mul_f32_e32 v100, v98, v100
	v_mul_f32_e32 v102, 0.5, v102
	v_pk_add_f32 v[98:99], v[132:133], v[134:135]
	v_bfi_b32 v135, s30, v125, v123
	v_mul_f32_e32 v99, v102, v99
	v_mul_f32_e32 v98, v98, v99
	v_mov_b32_e32 v132, v101
	v_cvt_pk_bf16_f32 v98, v100, v98
	v_mul_f32_e32 v99, 0.5, v103
	v_pk_add_f32 v[100:101], v[132:133], v[134:135]
	s_ashr_i32 s17, s16, 31
	v_mul_f32_e32 v99, v99, v101
	v_mul_f32_e32 v99, v100, v99
	v_cvt_pk_bf16_f32 v99, v109, v99
	v_or_b32_e32 v102, s14, v118
	v_mov_b64_e32 v[100:101], s[0:1]
	global_store_dwordx2 v[110:111], v[98:99], off offset:2144
	v_lshl_add_u64 v[98:99], s[16:17], 0, v[116:117]
	v_mad_u64_u32 v[100:101], s[16:17], v102, s25, v[100:101]
	v_mad_i32_i24 v101, s15, v157, v101
	v_lshl_add_u64 v[100:101], s[18:19], 1, v[100:101]
	v_lshl_add_u64 v[100:101], v[100:101], 0, v[114:115]
	v_add_co_u32_e32 v104, vcc, 0x1000, v100
	v_lshl_add_u64 v[98:99], v[98:99], 2, s[4:5]
	s_nop 0
	v_addc_co_u32_e32 v105, vcc, 0, v101, vcc
	global_load_dwordx2 v[176:177], v[104:105], off offset:4000
	global_load_dwordx2 v[178:179], v[104:105], off offset:4032
	global_load_dwordx2 v[180:181], v[104:105], off offset:4064
	global_load_dwordx2 v[104:105], v[104:105], off offset:3968
	v_mov_b32_e32 v103, s15
	global_load_dword v98, v[98:99], off offset:64
	s_waitcnt vmcnt(1)
	v_lshlrev_b32_e32 v99, 16, v104
	v_mul_f32_e32 v106, 0x3d372713, v99
	v_mul_f32_e32 v106, v106, v99
	v_fma_f32 v106, v106, v99, v99
	v_mul_f32_e32 v106, 0x3f4c422a, v106
	v_add_f32_e64 v107, |v106|, |v106|
	v_mul_f32_e32 v107, 0x3fb8aa3b, v107
	v_exp_f32_e32 v107, v107
	s_nop 0
	v_add_f32_e32 v107, 1.0, v107
	v_rcp_f32_e32 v107, v107
	s_nop 0
	v_fma_f32 v107, v107, -2.0, 1.0
	v_and_b32_e32 v104, 0xffff0000, v104
	v_mul_f32_e32 v108, 0x3d372713, v104
	v_mul_f32_e32 v108, v108, v104
	v_fma_f32 v108, v108, v104, v104
	v_mul_f32_e32 v108, 0x3f4c422a, v108
	v_add_f32_e64 v109, |v108|, |v108|
	v_mul_f32_e32 v109, 0x3fb8aa3b, v109
	v_exp_f32_e32 v109, v109
	s_nop 0
	v_add_f32_e32 v109, 1.0, v109
	v_rcp_f32_e32 v109, v109
	s_nop 0
	v_fma_f32 v109, v109, -2.0, 1.0
	v_lshlrev_b32_e32 v110, 16, v105
	v_mul_f32_e32 v111, 0x3d372713, v110
	v_mul_f32_e32 v111, v111, v110
	v_fma_f32 v111, v111, v110, v110
	v_mul_f32_e32 v111, 0x3f4c422a, v111
	v_add_f32_e64 v112, |v111|, |v111|
	v_mul_f32_e32 v112, 0x3fb8aa3b, v112
	v_exp_f32_e32 v112, v112
	s_nop 0
	v_add_f32_e32 v112, 1.0, v112
	v_rcp_f32_e32 v112, v112
	s_nop 0
	v_fma_f32 v112, v112, -2.0, 1.0
	v_and_b32_e32 v105, 0xffff0000, v105
	v_mul_f32_e32 v113, 0x3d372713, v105
	v_mul_f32_e32 v113, v113, v105
	v_fma_f32 v113, v113, v105, v105
	v_mul_f32_e32 v113, 0x3f4c422a, v113
	v_add_f32_e64 v123, |v113|, |v113|
	v_mul_f32_e32 v123, 0x3fb8aa3b, v123
	v_exp_f32_e32 v123, v123
	s_nop 0
	v_add_f32_e32 v123, 1.0, v123
	v_rcp_f32_e32 v123, v123
	s_nop 0
	v_fma_f32 v123, v123, -2.0, 1.0
	v_bfi_b32 v111, s30, v112, v111
	v_mul_f32_e32 v110, 0.5, v110
	v_add_f32_e32 v111, 1.0, v111
	v_mul_f32_e32 v110, v110, v111
	s_waitcnt vmcnt(0)
	v_add_f32_e32 v96, v96, v98
	v_mul_f32_e32 v110, v96, v110
	v_mul_f32_e32 v96, 0.5, v99
	v_bfi_b32 v99, s30, v107, v106
	v_add_f32_e32 v99, 1.0, v99
	v_mul_f32_e32 v96, v96, v99
	v_add_f32_e32 v94, v94, v98
	v_bfi_b32 v99, s30, v109, v108
	v_mov_b32_e32 v132, v95
	v_mul_f32_e32 v96, v94, v96
	v_mul_f32_e32 v104, 0.5, v104
	v_pk_add_f32 v[94:95], v[132:133], v[98:99]
	v_bfi_b32 v99, s30, v123, v113
	v_mul_f32_e32 v95, v104, v95
	v_mul_f32_e32 v94, v94, v95
	v_mov_b32_e32 v132, v97
	v_cvt_pk_bf16_f32 v96, v96, v94
	v_lshlrev_b64 v[94:95], 12, v[102:103]
	v_mul_f32_e32 v104, 0.5, v105
	v_pk_add_f32 v[102:103], v[132:133], v[98:99]
	v_lshl_add_u64 v[94:95], s[8:9], 0, v[94:95]
	v_mul_f32_e32 v97, v104, v103
	v_lshl_add_u64 v[94:95], s[18:19], 1, v[94:95]
	v_mul_f32_e32 v97, v102, v97
	v_lshl_add_u64 v[100:101], v[100:101], 0, s[10:11]
	v_lshl_add_u64 v[94:95], v[94:95], 0, v[114:115]
	v_cvt_pk_bf16_f32 v97, v110, v97
	global_store_dwordx2 v[94:95], v[96:97], off offset:2048
	v_mov_b64_e32 v[96:97], v[176:177]
	v_lshlrev_b32_e32 v99, 16, v96
	v_mul_f32_e32 v102, 0x3d372713, v99
	v_mul_f32_e32 v102, v102, v99
	v_fma_f32 v102, v102, v99, v99
	v_mul_f32_e32 v102, 0x3f4c422a, v102
	v_add_f32_e64 v103, |v102|, |v102|
	v_mul_f32_e32 v103, 0x3fb8aa3b, v103
	v_exp_f32_e32 v103, v103
	s_nop 0
	v_add_f32_e32 v103, 1.0, v103
	v_rcp_f32_e32 v103, v103
	s_nop 0
	v_fma_f32 v103, v103, -2.0, 1.0
	v_and_b32_e32 v96, 0xffff0000, v96
	v_mul_f32_e32 v104, 0x3d372713, v96
	v_mul_f32_e32 v104, v104, v96
	v_fma_f32 v104, v104, v96, v96
	v_mul_f32_e32 v104, 0x3f4c422a, v104
	v_add_f32_e64 v105, |v104|, |v104|
	v_mul_f32_e32 v105, 0x3fb8aa3b, v105
	v_exp_f32_e32 v105, v105
	s_nop 0
	v_add_f32_e32 v105, 1.0, v105
	v_rcp_f32_e32 v105, v105
	s_nop 0
	v_fma_f32 v105, v105, -2.0, 1.0
	v_lshlrev_b32_e32 v106, 16, v97
	v_mul_f32_e32 v107, 0x3d372713, v106
	v_mul_f32_e32 v107, v107, v106
	v_fma_f32 v107, v107, v106, v106
	v_mul_f32_e32 v107, 0x3f4c422a, v107
	v_add_f32_e64 v108, |v107|, |v107|
	v_mul_f32_e32 v108, 0x3fb8aa3b, v108
	v_exp_f32_e32 v108, v108
	s_nop 0
	v_add_f32_e32 v108, 1.0, v108
	v_rcp_f32_e32 v108, v108
	s_nop 0
	v_fma_f32 v108, v108, -2.0, 1.0
	v_and_b32_e32 v97, 0xffff0000, v97
	v_mul_f32_e32 v109, 0x3d372713, v97
	v_mul_f32_e32 v109, v109, v97
	v_fma_f32 v109, v109, v97, v97
	v_mul_f32_e32 v109, 0x3f4c422a, v109
	v_add_f32_e64 v110, |v109|, |v109|
	v_mul_f32_e32 v110, 0x3fb8aa3b, v110
	v_exp_f32_e32 v110, v110
	s_nop 0
	v_add_f32_e32 v110, 1.0, v110
	v_rcp_f32_e32 v110, v110
	s_nop 0
	v_fma_f32 v110, v110, -2.0, 1.0
	v_bfi_b32 v107, s30, v108, v107
	v_mul_f32_e32 v106, 0.5, v106
	v_add_f32_e32 v107, 1.0, v107
	v_mul_f32_e32 v106, v106, v107
	v_add_f32_e32 v92, v92, v98
	v_mul_f32_e32 v106, v92, v106
	v_mul_f32_e32 v92, 0.5, v99
	v_bfi_b32 v99, s30, v103, v102
	v_add_f32_e32 v99, 1.0, v99
	v_mul_f32_e32 v92, v92, v99
	v_add_f32_e32 v90, v90, v98
	v_bfi_b32 v99, s30, v105, v104
	v_mov_b32_e32 v132, v91
	v_mul_f32_e32 v92, v90, v92
	v_mul_f32_e32 v96, 0.5, v96
	v_pk_add_f32 v[90:91], v[132:133], v[98:99]
	v_bfi_b32 v99, s30, v110, v109
	v_mul_f32_e32 v91, v96, v91
	v_mul_f32_e32 v90, v90, v91
	v_mov_b32_e32 v132, v93
	v_cvt_pk_bf16_f32 v90, v92, v90
	v_mul_f32_e32 v91, 0.5, v97
	v_pk_add_f32 v[92:93], v[132:133], v[98:99]
	s_nop 0
	v_mul_f32_e32 v91, v91, v93
	v_mul_f32_e32 v91, v92, v91
	v_cvt_pk_bf16_f32 v91, v106, v91
	global_store_dwordx2 v[94:95], v[90:91], off offset:2080
	v_mov_b64_e32 v[90:91], v[178:179]
	v_lshlrev_b32_e32 v92, 16, v90
	v_mul_f32_e32 v93, 0x3d372713, v92
	v_mul_f32_e32 v93, v93, v92
	v_fma_f32 v93, v93, v92, v92
	v_mul_f32_e32 v93, 0x3f4c422a, v93
	v_add_f32_e64 v96, |v93|, |v93|
	v_mul_f32_e32 v96, 0x3fb8aa3b, v96
	v_exp_f32_e32 v96, v96
	s_nop 0
	v_add_f32_e32 v96, 1.0, v96
	v_rcp_f32_e32 v96, v96
	s_nop 0
	v_fma_f32 v96, v96, -2.0, 1.0
	v_and_b32_e32 v90, 0xffff0000, v90
	v_mul_f32_e32 v97, 0x3d372713, v90
	v_mul_f32_e32 v97, v97, v90
	v_fma_f32 v97, v97, v90, v90
	v_mul_f32_e32 v97, 0x3f4c422a, v97
	v_add_f32_e64 v99, |v97|, |v97|
	v_mul_f32_e32 v99, 0x3fb8aa3b, v99
	v_exp_f32_e32 v99, v99
	s_nop 0
	v_add_f32_e32 v99, 1.0, v99
	v_rcp_f32_e32 v99, v99
	s_nop 0
	v_fma_f32 v99, v99, -2.0, 1.0
	v_lshlrev_b32_e32 v102, 16, v91
	v_mul_f32_e32 v103, 0x3d372713, v102
	v_mul_f32_e32 v103, v103, v102
	v_fma_f32 v103, v103, v102, v102
	v_mul_f32_e32 v103, 0x3f4c422a, v103
	v_add_f32_e64 v104, |v103|, |v103|
	v_mul_f32_e32 v104, 0x3fb8aa3b, v104
	v_exp_f32_e32 v104, v104
	s_nop 0
	v_add_f32_e32 v104, 1.0, v104
	v_rcp_f32_e32 v104, v104
	s_nop 0
	v_fma_f32 v104, v104, -2.0, 1.0
	v_and_b32_e32 v91, 0xffff0000, v91
	v_mul_f32_e32 v105, 0x3d372713, v91
	v_mul_f32_e32 v105, v105, v91
	v_fma_f32 v105, v105, v91, v91
	v_mul_f32_e32 v105, 0x3f4c422a, v105
	v_add_f32_e64 v106, |v105|, |v105|
	v_mul_f32_e32 v106, 0x3fb8aa3b, v106
	v_exp_f32_e32 v106, v106
	s_nop 0
	v_add_f32_e32 v106, 1.0, v106
	v_rcp_f32_e32 v106, v106
	s_nop 0
	v_fma_f32 v106, v106, -2.0, 1.0
	v_bfi_b32 v103, s30, v104, v103
	v_mul_f32_e32 v102, 0.5, v102
	v_add_f32_e32 v103, 1.0, v103
	v_mul_f32_e32 v102, v102, v103
	v_add_f32_e32 v88, v88, v98
	v_mul_f32_e32 v102, v88, v102
	v_mul_f32_e32 v88, 0.5, v92
	v_bfi_b32 v92, s30, v96, v93
	v_add_f32_e32 v92, 1.0, v92
	v_mul_f32_e32 v88, v88, v92
	v_add_f32_e32 v86, v86, v98
	v_bfi_b32 v99, s30, v99, v97
	v_mov_b32_e32 v132, v87
	v_mul_f32_e32 v88, v86, v88
	v_mul_f32_e32 v90, 0.5, v90
	v_pk_add_f32 v[86:87], v[132:133], v[98:99]
	v_bfi_b32 v99, s30, v106, v105
	v_mul_f32_e32 v87, v90, v87
	v_mul_f32_e32 v86, v86, v87
	v_mov_b32_e32 v132, v89
	v_cvt_pk_bf16_f32 v86, v88, v86
	v_mul_f32_e32 v87, 0.5, v91
	v_pk_add_f32 v[88:89], v[132:133], v[98:99]
	s_nop 0
	v_mul_f32_e32 v87, v87, v89
	v_mul_f32_e32 v87, v88, v87
	v_cvt_pk_bf16_f32 v87, v102, v87
	global_store_dwordx2 v[94:95], v[86:87], off offset:2112
	v_mov_b64_e32 v[86:87], v[180:181]
	v_lshlrev_b32_e32 v88, 16, v86
	v_mul_f32_e32 v89, 0x3d372713, v88
	v_mul_f32_e32 v89, v89, v88
	v_fma_f32 v89, v89, v88, v88
	v_mul_f32_e32 v89, 0x3f4c422a, v89
	v_add_f32_e64 v90, |v89|, |v89|
	v_mul_f32_e32 v90, 0x3fb8aa3b, v90
	v_exp_f32_e32 v90, v90
	s_nop 0
	v_add_f32_e32 v90, 1.0, v90
	v_rcp_f32_e32 v90, v90
	s_nop 0
	v_fma_f32 v90, v90, -2.0, 1.0
	v_and_b32_e32 v86, 0xffff0000, v86
	v_mul_f32_e32 v91, 0x3d372713, v86
	v_mul_f32_e32 v91, v91, v86
	v_fma_f32 v91, v91, v86, v86
	v_mul_f32_e32 v91, 0x3f4c422a, v91
	v_add_f32_e64 v92, |v91|, |v91|
	v_mul_f32_e32 v92, 0x3fb8aa3b, v92
	v_exp_f32_e32 v92, v92
	s_nop 0
	v_add_f32_e32 v92, 1.0, v92
	v_rcp_f32_e32 v92, v92
	s_nop 0
	v_fma_f32 v92, v92, -2.0, 1.0
	v_lshlrev_b32_e32 v93, 16, v87
	v_mul_f32_e32 v96, 0x3d372713, v93
	v_mul_f32_e32 v96, v96, v93
	v_fma_f32 v96, v96, v93, v93
	v_mul_f32_e32 v96, 0x3f4c422a, v96
	v_add_f32_e64 v97, |v96|, |v96|
	v_mul_f32_e32 v97, 0x3fb8aa3b, v97
	v_exp_f32_e32 v97, v97
	s_nop 0
	v_add_f32_e32 v97, 1.0, v97
	v_rcp_f32_e32 v97, v97
	s_nop 0
	v_fma_f32 v97, v97, -2.0, 1.0
	v_and_b32_e32 v87, 0xffff0000, v87
	v_mul_f32_e32 v99, 0x3d372713, v87
	v_mul_f32_e32 v99, v99, v87
	v_fma_f32 v99, v99, v87, v87
	v_mul_f32_e32 v100, 0x3f4c422a, v99
	v_cmp_nlt_f32_e64 s[14:15], |v100|, s26
	s_and_saveexec_b64 s[16:17], s[14:15]
	s_xor_b64 s[14:15], exec, s[16:17]
	s_cbranch_execz .LBB0_1132
	v_add_f32_e64 v99, |v100|, |v100|
	v_mul_f32_e32 v101, 0x3fb8aa3b, v99
	v_rndne_f32_e32 v102, v101
	v_sub_f32_e32 v103, v101, v102
	v_fma_f32 v101, v99, s27, -v101
	v_fmac_f32_e32 v101, 0x32a5705f, v99
	v_add_f32_e32 v101, v103, v101
	v_cvt_i32_f32_e32 v102, v102
	v_exp_f32_e32 v101, v101
	v_cmp_ngt_f32_e32 vcc, s28, v99
	v_ldexp_f32 v101, v101, v102
	s_nop 0
	v_cndmask_b32_e32 v101, 0, v101, vcc
	v_cmp_nlt_f32_e32 vcc, s29, v99
	s_nop 1
	v_cndmask_b32_e32 v99, v158, v101, vcc
	v_add_f32_e32 v99, 1.0, v99
	v_rcp_f32_e32 v99, v99
	s_nop 0
	v_fma_f32 v101, v99, -2.0, 1.0

.LBB0_3324:
	ds_read_b64_tr_b16 v[82:83], v154
	ds_read_b64_tr_b16 v[86:87], v154 offset:32
	ds_read_b64_tr_b16 v[84:85], v145 offset:576
	ds_read_b64_tr_b16 v[88:89], v145 offset:608
	ds_read_b64_tr_b16 v[90:91], v154 offset:64
	ds_read_b64_tr_b16 v[92:93], v145 offset:640
	ds_read_b64_tr_b16 v[94:95], v154 offset:96
	ds_read_b64_tr_b16 v[96:97], v145 offset:672
	ds_read_b128 v[98:101], v155 offset:18432
	ds_read_b128 v[134:137], v155 offset:22784
	s_add_i32 s2, s8, s18
	s_ashr_i32 s3, s2, 31
	s_lshr_b32 s3, s3, 25
	s_waitcnt lgkmcnt(1)
	v_mfma_f32_16x16x32_bf16 v[102:105], v[82:85], v[98:101], 0
	s_add_i32 s3, s2, s3
	s_and_b32 s20, s3, 0xffffff80
	s_sub_i32 s2, s2, s20
	v_mfma_f32_16x16x32_bf16 v[106:109], v[86:89], v[98:101], 0
	s_ashr_i32 s21, s3, 7
	s_ashr_i32 s3, s2, 31
	s_lshl_b64 s[18:19], s[2:3], 7
	v_mfma_f32_16x16x32_bf16 v[110:113], v[90:93], v[98:101], 0
	s_lshl_b32 s22, s21, 6
	s_ashr_i32 s23, s22, 31
	v_mfma_f32_16x16x32_bf16 v[98:101], v[94:97], v[98:101], 0
	s_waitcnt lgkmcnt(0)
	v_mfma_f32_16x16x32_bf16 v[82:85], v[82:85], v[134:137], 0
	v_mfma_f32_16x16x32_bf16 v[86:89], v[86:89], v[134:137], 0
	v_mfma_f32_16x16x32_bf16 v[90:93], v[90:93], v[134:137], 0
	v_mfma_f32_16x16x32_bf16 v[94:97], v[94:97], v[134:137], 0
	ds_read_b64_tr_b16 v[134:135], v154 offset:4608
	ds_read_b64_tr_b16 v[136:137], v145 offset:5184
	ds_read_b64_tr_b16 v[138:139], v154 offset:4640
	ds_read_b64_tr_b16 v[140:141], v145 offset:5216
	ds_read_b64_tr_b16 v[160:161], v154 offset:4672
	ds_read_b64_tr_b16 v[162:163], v145 offset:5248
	ds_read_b64_tr_b16 v[164:165], v154 offset:4704
	ds_read_b64_tr_b16 v[166:167], v145 offset:5280
	ds_read_b128 v[168:171], v155 offset:18496
	s_waitcnt lgkmcnt(0)
	v_mfma_f32_16x16x32_bf16 v[102:105], v[134:137], v[168:171], v[102:105]
	v_mfma_f32_16x16x32_bf16 v[106:109], v[138:141], v[168:171], v[106:109]
	v_mfma_f32_16x16x32_bf16 v[110:113], v[160:163], v[168:171], v[110:113]
	v_mfma_f32_16x16x32_bf16 v[98:101], v[164:167], v[168:171], v[98:101]
	ds_read_b128 v[168:171], v155 offset:22848
	s_waitcnt lgkmcnt(0)
	v_mfma_f32_16x16x32_bf16 v[82:85], v[134:137], v[168:171], v[82:85]
	v_mfma_f32_16x16x32_bf16 v[86:89], v[138:141], v[168:171], v[86:89]
	v_mfma_f32_16x16x32_bf16 v[90:93], v[160:163], v[168:171], v[90:93]
	v_mfma_f32_16x16x32_bf16 v[94:97], v[164:167], v[168:171], v[94:97]
	ds_read_b64_tr_b16 v[134:135], v154 offset:9216
	ds_read_b64_tr_b16 v[136:137], v145 offset:9792
	ds_read_b64_tr_b16 v[138:139], v154 offset:9248
	ds_read_b64_tr_b16 v[140:141], v145 offset:9824
	ds_read_b64_tr_b16 v[160:161], v154 offset:9280
	ds_read_b64_tr_b16 v[162:163], v145 offset:9856
	ds_read_b64_tr_b16 v[164:165], v154 offset:9312
	ds_read_b64_tr_b16 v[166:167], v145 offset:9888
	ds_read_b128 v[168:171], v155 offset:18560
	s_waitcnt lgkmcnt(0)
	v_mfma_f32_16x16x32_bf16 v[172:175], v[160:163], v[168:171], v[110:113]
	s_nop 2
	ds_read_b128 v[110:113], v155 offset:22912
	v_mfma_f32_16x16x32_bf16 v[102:105], v[134:137], v[168:171], v[102:105]
	v_mfma_f32_16x16x32_bf16 v[106:109], v[138:141], v[168:171], v[106:109]
	v_mfma_f32_16x16x32_bf16 v[98:101], v[164:167], v[168:171], v[98:101]
	s_waitcnt lgkmcnt(0)
	v_mfma_f32_16x16x32_bf16 v[82:85], v[134:137], v[110:113], v[82:85]
	v_mfma_f32_16x16x32_bf16 v[86:89], v[138:141], v[110:113], v[86:89]
	v_mfma_f32_16x16x32_bf16 v[134:137], v[160:163], v[110:113], v[90:93]
	v_mfma_f32_16x16x32_bf16 v[138:141], v[164:167], v[110:113], v[94:97]
	s_nop 1
	ds_read_b64_tr_b16 v[90:91], v154 offset:13824
	ds_read_b64_tr_b16 v[92:93], v145 offset:14400
	ds_read_b64_tr_b16 v[160:161], v154 offset:13856
	ds_read_b64_tr_b16 v[162:163], v145 offset:14432
	ds_read_b64_tr_b16 v[164:165], v154 offset:13888
	ds_read_b64_tr_b16 v[166:167], v145 offset:14464
	ds_read_b64_tr_b16 v[168:169], v154 offset:13920
	ds_read_b64_tr_b16 v[170:171], v145 offset:14496
	ds_read_b128 v[94:97], v155 offset:18624
	s_waitcnt lgkmcnt(0)
	v_mfma_f32_16x16x32_bf16 v[110:113], v[90:93], v[94:97], v[102:105]
	v_mfma_f32_16x16x32_bf16 v[102:105], v[164:167], v[94:97], v[172:175]
	s_nop 2
	ds_read_b128 v[172:175], v155 offset:22976
	v_mfma_f32_16x16x32_bf16 v[106:109], v[160:163], v[94:97], v[106:109]
	v_mfma_f32_16x16x32_bf16 v[98:101], v[168:171], v[94:97], v[98:101]
	s_waitcnt lgkmcnt(0)
	v_mfma_f32_16x16x32_bf16 v[94:97], v[90:93], v[172:175], v[82:85]
	v_mfma_f32_16x16x32_bf16 v[90:93], v[160:163], v[172:175], v[86:89]
	v_mfma_f32_16x16x32_bf16 v[86:89], v[164:167], v[172:175], v[134:137]
	v_mfma_f32_16x16x32_bf16 v[82:85], v[168:171], v[172:175], v[138:141]
	s_nop 1
	v_mov_b64_e32 v[136:137], s[0:1]
	v_or_b32_e32 v134, s20, v116
	v_ashrrev_i32_e32 v135, 31, v134
	v_or_b32_e32 v138, s18, v116
	v_mad_u64_u32 v[136:137], s[2:3], v138, s11, v[136:137]
	v_mad_i32_i24 v137, s19, v157, v137
	v_lshl_add_u64 v[136:137], s[22:23], 1, v[136:137]
	v_lshl_add_u64 v[136:137], v[136:137], 0, v[114:115]
	v_add_co_u32_e32 v140, vcc, 0x1000, v136
	v_lshl_add_u64 v[134:135], v[134:135], 2, s[6:7]
	s_nop 0
	v_addc_co_u32_e32 v141, vcc, 0, v137, vcc
	global_load_dwordx2 v[176:177], v[140:141], off offset:4000
	global_load_dwordx2 v[178:179], v[140:141], off offset:4032
	global_load_dwordx2 v[180:181], v[140:141], off offset:4064
	global_load_dwordx2 v[140:141], v[140:141], off offset:3968
	v_mov_b32_e32 v139, s19
	global_load_dword v134, v[134:135], off
	s_waitcnt vmcnt(1)
	v_lshlrev_b32_e32 v123, 16, v140
	v_mul_f32_e32 v125, 0x3d372713, v123
	v_mul_f32_e32 v125, v125, v123
	v_fma_f32 v125, v125, v123, v123
	v_mul_f32_e32 v125, 0x3f4c422a, v125
	v_add_f32_e64 v127, |v125|, |v125|
	v_mul_f32_e32 v127, 0x3fb8aa3b, v127
	v_exp_f32_e32 v127, v127
	s_nop 0
	v_add_f32_e32 v127, 1.0, v127
	v_rcp_f32_e32 v127, v127
	s_nop 0
	v_fma_f32 v127, v127, -2.0, 1.0
	v_and_b32_e32 v129, 0xffff0000, v140
	v_mul_f32_e32 v131, 0x3d372713, v129
	v_mul_f32_e32 v131, v131, v129
	v_fma_f32 v131, v131, v129, v129
	v_mul_f32_e32 v131, 0x3f4c422a, v131
	v_add_f32_e64 v132, |v131|, |v131|
	v_mul_f32_e32 v132, 0x3fb8aa3b, v132
	v_exp_f32_e32 v132, v132
	s_nop 0
	v_add_f32_e32 v132, 1.0, v132
	v_rcp_f32_e32 v132, v132
	s_nop 0
	v_fma_f32 v132, v132, -2.0, 1.0
	v_lshlrev_b32_e32 v135, 16, v141
	v_mul_f32_e32 v140, 0x3d372713, v135
	v_mul_f32_e32 v140, v140, v135
	v_fma_f32 v140, v140, v135, v135
	v_mul_f32_e32 v140, 0x3f4c422a, v140
	v_add_f32_e64 v159, |v140|, |v140|
	v_mul_f32_e32 v159, 0x3fb8aa3b, v159
	v_exp_f32_e32 v159, v159
	s_nop 0
	v_add_f32_e32 v159, 1.0, v159
	v_rcp_f32_e32 v159, v159
	s_nop 0
	v_fma_f32 v159, v159, -2.0, 1.0
	v_and_b32_e32 v141, 0xffff0000, v141
	v_mul_f32_e32 v160, 0x3d372713, v141
	v_mul_f32_e32 v160, v160, v141
	v_fma_f32 v160, v160, v141, v141
	v_mul_f32_e32 v160, 0x3f4c422a, v160
	v_add_f32_e64 v161, |v160|, |v160|
	v_mul_f32_e32 v161, 0x3fb8aa3b, v161
	v_exp_f32_e32 v161, v161
	s_nop 0
	v_add_f32_e32 v161, 1.0, v161
	v_rcp_f32_e32 v161, v161
	s_nop 0
	v_fma_f32 v161, v161, -2.0, 1.0
	v_bfi_b32 v140, s30, v159, v140
	v_mul_f32_e32 v135, 0.5, v135
	v_add_f32_e32 v140, 1.0, v140
	v_mul_f32_e32 v135, v135, v140
	s_waitcnt vmcnt(0)
	v_add_f32_e32 v112, v112, v134
	v_mul_f32_e32 v140, v112, v135
	v_mul_f32_e32 v112, 0.5, v123
	v_bfi_b32 v123, s30, v127, v125
	v_add_f32_e32 v123, 1.0, v123
	v_mul_f32_e32 v112, v112, v123
	v_add_f32_e32 v110, v110, v134
	v_bfi_b32 v135, s30, v132, v131
	v_mov_b32_e32 v132, v111
	v_mul_f32_e32 v112, v110, v112
	v_mul_f32_e32 v123, 0.5, v129
	v_pk_add_f32 v[110:111], v[132:133], v[134:135]
	v_bfi_b32 v135, s30, v161, v160
	v_mul_f32_e32 v111, v123, v111
	v_mul_f32_e32 v110, v110, v111
	v_mov_b32_e32 v132, v113
	v_cvt_pk_bf16_f32 v112, v112, v110
	v_lshlrev_b64 v[110:111], 12, v[138:139]
	v_mul_f32_e32 v123, 0.5, v141
	v_pk_add_f32 v[138:139], v[132:133], v[134:135]
	v_lshl_add_u64 v[110:111], s[12:13], 0, v[110:111]
	v_mul_f32_e32 v113, v123, v139
	v_lshl_add_u64 v[110:111], s[22:23], 1, v[110:111]
	v_mul_f32_e32 v113, v138, v113
	v_lshl_add_u64 v[136:137], v[136:137], 0, s[14:15]
	v_lshl_add_u64 v[110:111], v[110:111], 0, v[114:115]
	v_cvt_pk_bf16_f32 v113, v140, v113
	global_store_dwordx2 v[110:111], v[112:113], off offset:2048
	v_mov_b64_e32 v[112:113], v[176:177]
	v_lshlrev_b32_e32 v123, 16, v112
	v_mul_f32_e32 v125, 0x3d372713, v123
	v_mul_f32_e32 v125, v125, v123
	v_fma_f32 v125, v125, v123, v123
	v_mul_f32_e32 v125, 0x3f4c422a, v125
	v_add_f32_e64 v127, |v125|, |v125|
	v_mul_f32_e32 v127, 0x3fb8aa3b, v127
	v_exp_f32_e32 v127, v127
	s_nop 0
	v_add_f32_e32 v127, 1.0, v127
	v_rcp_f32_e32 v127, v127
	s_nop 0
	v_fma_f32 v127, v127, -2.0, 1.0
	v_and_b32_e32 v112, 0xffff0000, v112
	v_mul_f32_e32 v129, 0x3d372713, v112
	v_mul_f32_e32 v129, v129, v112
	v_fma_f32 v129, v129, v112, v112
	v_mul_f32_e32 v129, 0x3f4c422a, v129
	v_add_f32_e64 v131, |v129|, |v129|
	v_mul_f32_e32 v131, 0x3fb8aa3b, v131
	v_exp_f32_e32 v131, v131
	s_nop 0
	v_add_f32_e32 v131, 1.0, v131
	v_rcp_f32_e32 v131, v131
	s_nop 0
	v_fma_f32 v131, v131, -2.0, 1.0
	v_lshlrev_b32_e32 v132, 16, v113
	v_mul_f32_e32 v135, 0x3d372713, v132
	v_mul_f32_e32 v135, v135, v132
	v_fma_f32 v135, v135, v132, v132
	v_mul_f32_e32 v135, 0x3f4c422a, v135
	v_add_f32_e64 v138, |v135|, |v135|
	v_mul_f32_e32 v138, 0x3fb8aa3b, v138
	v_exp_f32_e32 v138, v138
	s_nop 0
	v_add_f32_e32 v138, 1.0, v138
	v_rcp_f32_e32 v138, v138
	s_nop 0
	v_fma_f32 v138, v138, -2.0, 1.0
	v_and_b32_e32 v113, 0xffff0000, v113
	v_mul_f32_e32 v139, 0x3d372713, v113
	v_mul_f32_e32 v139, v139, v113
	v_fma_f32 v139, v139, v113, v113
	v_mul_f32_e32 v139, 0x3f4c422a, v139
	v_add_f32_e64 v140, |v139|, |v139|
	v_mul_f32_e32 v140, 0x3fb8aa3b, v140
	v_exp_f32_e32 v140, v140
	s_nop 0
	v_add_f32_e32 v140, 1.0, v140
	v_rcp_f32_e32 v140, v140
	s_nop 0
	v_fma_f32 v140, v140, -2.0, 1.0
	v_bfi_b32 v135, s30, v138, v135
	v_mul_f32_e32 v132, 0.5, v132
	v_add_f32_e32 v135, 1.0, v135
	v_mul_f32_e32 v132, v132, v135
	v_add_f32_e32 v108, v108, v134
	v_mul_f32_e32 v138, v108, v132
	v_mul_f32_e32 v108, 0.5, v123
	v_bfi_b32 v123, s30, v127, v125
	v_add_f32_e32 v123, 1.0, v123
	v_mul_f32_e32 v108, v108, v123
	v_add_f32_e32 v106, v106, v134
	v_bfi_b32 v135, s30, v131, v129
	v_mov_b32_e32 v132, v107
	v_mul_f32_e32 v108, v106, v108
	v_mul_f32_e32 v112, 0.5, v112
	v_pk_add_f32 v[106:107], v[132:133], v[134:135]
	v_bfi_b32 v135, s30, v140, v139
	v_mul_f32_e32 v107, v112, v107
	v_mul_f32_e32 v106, v106, v107
	v_mov_b32_e32 v132, v109
	v_cvt_pk_bf16_f32 v106, v108, v106
	v_mul_f32_e32 v107, 0.5, v113
	v_pk_add_f32 v[108:109], v[132:133], v[134:135]
	s_nop 0
	v_mul_f32_e32 v107, v107, v109
	v_mul_f32_e32 v107, v108, v107
	v_cvt_pk_bf16_f32 v107, v138, v107
	global_store_dwordx2 v[110:111], v[106:107], off offset:2080
	v_mov_b64_e32 v[106:107], v[178:179]
	v_lshlrev_b32_e32 v108, 16, v106
	v_mul_f32_e32 v109, 0x3d372713, v108
	v_mul_f32_e32 v109, v109, v108
	v_fma_f32 v109, v109, v108, v108
	v_mul_f32_e32 v109, 0x3f4c422a, v109
	v_add_f32_e64 v112, |v109|, |v109|
	v_mul_f32_e32 v112, 0x3fb8aa3b, v112
	v_exp_f32_e32 v112, v112
	s_nop 0
	v_add_f32_e32 v112, 1.0, v112
	v_rcp_f32_e32 v112, v112
	s_nop 0
	v_fma_f32 v112, v112, -2.0, 1.0
	v_and_b32_e32 v106, 0xffff0000, v106
	v_mul_f32_e32 v113, 0x3d372713, v106
	v_mul_f32_e32 v113, v113, v106
	v_fma_f32 v113, v113, v106, v106
	v_mul_f32_e32 v113, 0x3f4c422a, v113
	v_add_f32_e64 v123, |v113|, |v113|
	v_mul_f32_e32 v123, 0x3fb8aa3b, v123
	v_exp_f32_e32 v123, v123
	s_nop 0
	v_add_f32_e32 v123, 1.0, v123
	v_rcp_f32_e32 v123, v123
	s_nop 0
	v_fma_f32 v123, v123, -2.0, 1.0
	v_lshlrev_b32_e32 v125, 16, v107
	v_mul_f32_e32 v127, 0x3d372713, v125
	v_mul_f32_e32 v127, v127, v125
	v_fma_f32 v127, v127, v125, v125
	v_mul_f32_e32 v127, 0x3f4c422a, v127
	v_add_f32_e64 v129, |v127|, |v127|
	v_mul_f32_e32 v129, 0x3fb8aa3b, v129
	v_exp_f32_e32 v129, v129
	s_nop 0
	v_add_f32_e32 v129, 1.0, v129
	v_rcp_f32_e32 v129, v129
	s_nop 0
	v_fma_f32 v129, v129, -2.0, 1.0
	v_and_b32_e32 v107, 0xffff0000, v107
	v_mul_f32_e32 v131, 0x3d372713, v107
	v_mul_f32_e32 v131, v131, v107
	v_fma_f32 v131, v131, v107, v107
	v_mul_f32_e32 v131, 0x3f4c422a, v131
	v_add_f32_e64 v138, |v131|, |v131|
	v_mul_f32_e32 v138, 0x3fb8aa3b, v138
	v_exp_f32_e32 v138, v138
	s_nop 0
	v_add_f32_e32 v138, 1.0, v138
	v_rcp_f32_e32 v138, v138
	s_nop 0
	v_fma_f32 v138, v138, -2.0, 1.0
	v_bfi_b32 v127, s30, v129, v127
	v_mul_f32_e32 v125, 0.5, v125
	v_add_f32_e32 v127, 1.0, v127
	v_mul_f32_e32 v125, v125, v127
	v_add_f32_e32 v104, v104, v134
	v_mul_f32_e32 v125, v104, v125
	v_mul_f32_e32 v104, 0.5, v108
	v_bfi_b32 v108, s30, v112, v109
	v_add_f32_e32 v108, 1.0, v108
	v_mul_f32_e32 v104, v104, v108
	v_add_f32_e32 v102, v102, v134
	v_bfi_b32 v135, s30, v123, v113
	v_mov_b32_e32 v132, v103
	v_mul_f32_e32 v104, v102, v104
	v_mul_f32_e32 v106, 0.5, v106
	v_pk_add_f32 v[102:103], v[132:133], v[134:135]
	v_bfi_b32 v135, s30, v138, v131
	v_mul_f32_e32 v103, v106, v103
	v_mul_f32_e32 v102, v102, v103
	v_mov_b32_e32 v132, v105
	v_cvt_pk_bf16_f32 v102, v104, v102
	v_mul_f32_e32 v103, 0.5, v107
	v_pk_add_f32 v[104:105], v[132:133], v[134:135]
	s_nop 0
	v_mul_f32_e32 v103, v103, v105
	v_mul_f32_e32 v103, v104, v103
	v_cvt_pk_bf16_f32 v103, v125, v103
	global_store_dwordx2 v[110:111], v[102:103], off offset:2112
	v_mov_b64_e32 v[102:103], v[180:181]
	v_lshlrev_b32_e32 v104, 16, v102
	v_mul_f32_e32 v105, 0x3d372713, v104
	v_mul_f32_e32 v105, v105, v104
	v_fma_f32 v105, v105, v104, v104
	v_mul_f32_e32 v105, 0x3f4c422a, v105
	v_add_f32_e64 v106, |v105|, |v105|
	v_mul_f32_e32 v106, 0x3fb8aa3b, v106
	v_exp_f32_e32 v106, v106
	s_nop 0
	v_add_f32_e32 v106, 1.0, v106
	v_rcp_f32_e32 v106, v106
	s_nop 0
	v_fma_f32 v106, v106, -2.0, 1.0
	v_and_b32_e32 v102, 0xffff0000, v102
	v_mul_f32_e32 v107, 0x3d372713, v102
	v_mul_f32_e32 v107, v107, v102
	v_fma_f32 v107, v107, v102, v102
	v_mul_f32_e32 v107, 0x3f4c422a, v107
	v_add_f32_e64 v108, |v107|, |v107|
	v_mul_f32_e32 v108, 0x3fb8aa3b, v108
	v_exp_f32_e32 v108, v108
	s_nop 0
	v_add_f32_e32 v108, 1.0, v108
	v_rcp_f32_e32 v108, v108
	s_nop 0
	v_fma_f32 v108, v108, -2.0, 1.0
	v_lshlrev_b32_e32 v109, 16, v103
	v_mul_f32_e32 v112, 0x3d372713, v109
	v_mul_f32_e32 v112, v112, v109
	v_fma_f32 v112, v112, v109, v109
	v_mul_f32_e32 v112, 0x3f4c422a, v112
	v_add_f32_e64 v113, |v112|, |v112|
	v_mul_f32_e32 v113, 0x3fb8aa3b, v113
	v_exp_f32_e32 v113, v113
	s_nop 0
	v_add_f32_e32 v113, 1.0, v113
	v_rcp_f32_e32 v113, v113
	s_nop 0
	v_fma_f32 v113, v113, -2.0, 1.0
	v_and_b32_e32 v103, 0xffff0000, v103
	v_mul_f32_e32 v123, 0x3d372713, v103
	v_mul_f32_e32 v123, v123, v103
	v_fma_f32 v123, v123, v103, v103
	v_mul_f32_e32 v123, 0x3f4c422a, v123
	v_add_f32_e64 v125, |v123|, |v123|
	v_mul_f32_e32 v125, 0x3fb8aa3b, v125
	v_exp_f32_e32 v125, v125
	s_nop 0
	v_add_f32_e32 v125, 1.0, v125
	v_rcp_f32_e32 v125, v125
	s_nop 0
	v_fma_f32 v125, v125, -2.0, 1.0
	v_bfi_b32 v112, s30, v113, v112
	v_mul_f32_e32 v109, 0.5, v109
	v_add_f32_e32 v112, 1.0, v112
	v_mul_f32_e32 v109, v109, v112
	v_add_f32_e32 v100, v100, v134
	v_mul_f32_e32 v109, v100, v109
	v_mul_f32_e32 v100, 0.5, v104
	v_bfi_b32 v104, s30, v106, v105
	v_add_f32_e32 v104, 1.0, v104
	v_mul_f32_e32 v100, v100, v104
	v_add_f32_e32 v98, v98, v134
	v_bfi_b32 v135, s30, v108, v107
	v_mov_b32_e32 v132, v99
	v_mul_f32_e32 v100, v98, v100
	v_mul_f32_e32 v102, 0.5, v102
	v_pk_add_f32 v[98:99], v[132:133], v[134:135]
	v_bfi_b32 v135, s30, v125, v123
	v_mul_f32_e32 v99, v102, v99
	v_mul_f32_e32 v98, v98, v99
	v_mov_b32_e32 v132, v101
	v_cvt_pk_bf16_f32 v98, v100, v98
	v_mul_f32_e32 v99, 0.5, v103
	v_pk_add_f32 v[100:101], v[132:133], v[134:135]
	v_or_b32_e32 v102, s18, v118
	v_mul_f32_e32 v99, v99, v101
	v_mul_f32_e32 v99, v100, v99
	v_mov_b64_e32 v[100:101], s[0:1]
	v_mad_u64_u32 v[100:101], s[2:3], v102, s11, v[100:101]
	v_mad_i32_i24 v101, s19, v157, v101
	v_lshl_add_u64 v[100:101], s[22:23], 1, v[100:101]
	v_lshl_add_u64 v[100:101], v[100:101], 0, v[114:115]
	v_add_co_u32_e32 v104, vcc, 0x1000, v100
	v_cvt_pk_bf16_f32 v99, v109, v99
	s_nop 0
	v_addc_co_u32_e32 v105, vcc, 0, v101, vcc
	global_load_dwordx2 v[176:177], v[104:105], off offset:4000
	global_load_dwordx2 v[178:179], v[104:105], off offset:4032
	global_load_dwordx2 v[180:181], v[104:105], off offset:4064
	global_load_dwordx2 v[104:105], v[104:105], off offset:3968
	s_ashr_i32 s21, s20, 31
	global_store_dwordx2 v[110:111], v[98:99], off offset:2144
	v_lshl_add_u64 v[98:99], s[20:21], 0, v[116:117]
	v_lshl_add_u64 v[98:99], v[98:99], 2, s[6:7]
	global_load_dword v98, v[98:99], off offset:64
	v_mov_b32_e32 v103, s19
	s_waitcnt vmcnt(2)
	v_lshlrev_b32_e32 v99, 16, v104
	v_mul_f32_e32 v106, 0x3d372713, v99
	v_mul_f32_e32 v106, v106, v99
	v_fma_f32 v106, v106, v99, v99
	v_mul_f32_e32 v106, 0x3f4c422a, v106
	v_add_f32_e64 v107, |v106|, |v106|
	v_mul_f32_e32 v107, 0x3fb8aa3b, v107
	v_exp_f32_e32 v107, v107
	s_nop 0
	v_add_f32_e32 v107, 1.0, v107
	v_rcp_f32_e32 v107, v107
	s_nop 0
	v_fma_f32 v107, v107, -2.0, 1.0
	v_and_b32_e32 v104, 0xffff0000, v104
	v_mul_f32_e32 v108, 0x3d372713, v104
	v_mul_f32_e32 v108, v108, v104
	v_fma_f32 v108, v108, v104, v104
	v_mul_f32_e32 v108, 0x3f4c422a, v108
	v_add_f32_e64 v109, |v108|, |v108|
	v_mul_f32_e32 v109, 0x3fb8aa3b, v109
	v_exp_f32_e32 v109, v109
	s_nop 0
	v_add_f32_e32 v109, 1.0, v109
	v_rcp_f32_e32 v109, v109
	s_nop 0
	v_fma_f32 v109, v109, -2.0, 1.0
	v_lshlrev_b32_e32 v110, 16, v105
	v_mul_f32_e32 v111, 0x3d372713, v110
	v_mul_f32_e32 v111, v111, v110
	v_fma_f32 v111, v111, v110, v110
	v_mul_f32_e32 v111, 0x3f4c422a, v111
	v_add_f32_e64 v112, |v111|, |v111|
	v_mul_f32_e32 v112, 0x3fb8aa3b, v112
	v_exp_f32_e32 v112, v112
	s_nop 0
	v_add_f32_e32 v112, 1.0, v112
	v_rcp_f32_e32 v112, v112
	s_nop 0
	v_fma_f32 v112, v112, -2.0, 1.0
	v_and_b32_e32 v105, 0xffff0000, v105
	v_mul_f32_e32 v113, 0x3d372713, v105
	v_mul_f32_e32 v113, v113, v105
	v_fma_f32 v113, v113, v105, v105
	v_mul_f32_e32 v113, 0x3f4c422a, v113
	v_add_f32_e64 v123, |v113|, |v113|
	v_mul_f32_e32 v123, 0x3fb8aa3b, v123
	v_exp_f32_e32 v123, v123
	s_nop 0
	v_add_f32_e32 v123, 1.0, v123
	v_rcp_f32_e32 v123, v123
	s_nop 0
	v_fma_f32 v123, v123, -2.0, 1.0
	v_bfi_b32 v111, s30, v112, v111
	v_mul_f32_e32 v110, 0.5, v110
	v_add_f32_e32 v111, 1.0, v111
	v_mul_f32_e32 v110, v110, v111
	s_waitcnt vmcnt(0)
	v_add_f32_e32 v96, v96, v98
	v_mul_f32_e32 v110, v96, v110
	v_mul_f32_e32 v96, 0.5, v99
	v_bfi_b32 v99, s30, v107, v106
	v_add_f32_e32 v99, 1.0, v99
	v_mul_f32_e32 v96, v96, v99
	v_add_f32_e32 v94, v94, v98
	v_bfi_b32 v99, s30, v109, v108
	v_mov_b32_e32 v132, v95
	v_mul_f32_e32 v96, v94, v96
	v_mul_f32_e32 v104, 0.5, v104
	v_pk_add_f32 v[94:95], v[132:133], v[98:99]
	v_bfi_b32 v99, s30, v123, v113
	v_mul_f32_e32 v95, v104, v95
	v_mul_f32_e32 v94, v94, v95
	v_mov_b32_e32 v132, v97
	v_cvt_pk_bf16_f32 v96, v96, v94
	v_lshlrev_b64 v[94:95], 12, v[102:103]
	v_mul_f32_e32 v104, 0.5, v105
	v_pk_add_f32 v[102:103], v[132:133], v[98:99]
	v_lshl_add_u64 v[94:95], s[12:13], 0, v[94:95]
	v_mul_f32_e32 v97, v104, v103
	v_lshl_add_u64 v[94:95], s[22:23], 1, v[94:95]
	v_mul_f32_e32 v97, v102, v97
	v_lshl_add_u64 v[100:101], v[100:101], 0, s[14:15]
	v_lshl_add_u64 v[94:95], v[94:95], 0, v[114:115]
	v_cvt_pk_bf16_f32 v97, v110, v97
	global_store_dwordx2 v[94:95], v[96:97], off offset:2048
	v_mov_b64_e32 v[96:97], v[176:177]
	v_lshlrev_b32_e32 v99, 16, v96
	v_mul_f32_e32 v102, 0x3d372713, v99
	v_mul_f32_e32 v102, v102, v99
	v_fma_f32 v102, v102, v99, v99
	v_mul_f32_e32 v102, 0x3f4c422a, v102
	v_add_f32_e64 v103, |v102|, |v102|
	v_mul_f32_e32 v103, 0x3fb8aa3b, v103
	v_exp_f32_e32 v103, v103
	s_nop 0
	v_add_f32_e32 v103, 1.0, v103
	v_rcp_f32_e32 v103, v103
	s_nop 0
	v_fma_f32 v103, v103, -2.0, 1.0
	v_and_b32_e32 v96, 0xffff0000, v96
	v_mul_f32_e32 v104, 0x3d372713, v96
	v_mul_f32_e32 v104, v104, v96
	v_fma_f32 v104, v104, v96, v96
	v_mul_f32_e32 v104, 0x3f4c422a, v104
	v_add_f32_e64 v105, |v104|, |v104|
	v_mul_f32_e32 v105, 0x3fb8aa3b, v105
	v_exp_f32_e32 v105, v105
	s_nop 0
	v_add_f32_e32 v105, 1.0, v105
	v_rcp_f32_e32 v105, v105
	s_nop 0
	v_fma_f32 v105, v105, -2.0, 1.0
	v_lshlrev_b32_e32 v106, 16, v97
	v_mul_f32_e32 v107, 0x3d372713, v106
	v_mul_f32_e32 v107, v107, v106
	v_fma_f32 v107, v107, v106, v106
	v_mul_f32_e32 v107, 0x3f4c422a, v107
	v_add_f32_e64 v108, |v107|, |v107|
	v_mul_f32_e32 v108, 0x3fb8aa3b, v108
	v_exp_f32_e32 v108, v108
	s_nop 0
	v_add_f32_e32 v108, 1.0, v108
	v_rcp_f32_e32 v108, v108
	s_nop 0
	v_fma_f32 v108, v108, -2.0, 1.0
	v_and_b32_e32 v97, 0xffff0000, v97
	v_mul_f32_e32 v109, 0x3d372713, v97
	v_mul_f32_e32 v109, v109, v97
	v_fma_f32 v109, v109, v97, v97
	v_mul_f32_e32 v109, 0x3f4c422a, v109
	v_add_f32_e64 v110, |v109|, |v109|
	v_mul_f32_e32 v110, 0x3fb8aa3b, v110
	v_exp_f32_e32 v110, v110
	s_nop 0
	v_add_f32_e32 v110, 1.0, v110
	v_rcp_f32_e32 v110, v110
	s_nop 0
	v_fma_f32 v110, v110, -2.0, 1.0
	v_bfi_b32 v107, s30, v108, v107
	v_mul_f32_e32 v106, 0.5, v106
	v_add_f32_e32 v107, 1.0, v107
	v_mul_f32_e32 v106, v106, v107
	v_add_f32_e32 v92, v92, v98
	v_mul_f32_e32 v106, v92, v106
	v_mul_f32_e32 v92, 0.5, v99
	v_bfi_b32 v99, s30, v103, v102
	v_add_f32_e32 v99, 1.0, v99
	v_mul_f32_e32 v92, v92, v99
	v_add_f32_e32 v90, v90, v98
	v_bfi_b32 v99, s30, v105, v104
	v_mov_b32_e32 v132, v91
	v_mul_f32_e32 v92, v90, v92
	v_mul_f32_e32 v96, 0.5, v96
	v_pk_add_f32 v[90:91], v[132:133], v[98:99]
	v_bfi_b32 v99, s30, v110, v109
	v_mul_f32_e32 v91, v96, v91
	v_mul_f32_e32 v90, v90, v91
	v_mov_b32_e32 v132, v93
	v_cvt_pk_bf16_f32 v90, v92, v90
	v_mul_f32_e32 v91, 0.5, v97
	v_pk_add_f32 v[92:93], v[132:133], v[98:99]
	s_nop 0
	v_mul_f32_e32 v91, v91, v93
	v_mul_f32_e32 v91, v92, v91
	v_cvt_pk_bf16_f32 v91, v106, v91
	global_store_dwordx2 v[94:95], v[90:91], off offset:2080
	v_mov_b64_e32 v[90:91], v[178:179]
	v_lshlrev_b32_e32 v92, 16, v90
	v_mul_f32_e32 v93, 0x3d372713, v92
	v_mul_f32_e32 v93, v93, v92
	v_fma_f32 v93, v93, v92, v92
	v_mul_f32_e32 v93, 0x3f4c422a, v93
	v_add_f32_e64 v96, |v93|, |v93|
	v_mul_f32_e32 v96, 0x3fb8aa3b, v96
	v_exp_f32_e32 v96, v96
	s_nop 0
	v_add_f32_e32 v96, 1.0, v96
	v_rcp_f32_e32 v96, v96
	s_nop 0
	v_fma_f32 v96, v96, -2.0, 1.0
	v_and_b32_e32 v90, 0xffff0000, v90
	v_mul_f32_e32 v97, 0x3d372713, v90
	v_mul_f32_e32 v97, v97, v90
	v_fma_f32 v97, v97, v90, v90
	v_mul_f32_e32 v97, 0x3f4c422a, v97
	v_add_f32_e64 v99, |v97|, |v97|
	v_mul_f32_e32 v99, 0x3fb8aa3b, v99
	v_exp_f32_e32 v99, v99
	s_nop 0
	v_add_f32_e32 v99, 1.0, v99
	v_rcp_f32_e32 v99, v99
	s_nop 0
	v_fma_f32 v99, v99, -2.0, 1.0
	v_lshlrev_b32_e32 v102, 16, v91
	v_mul_f32_e32 v103, 0x3d372713, v102
	v_mul_f32_e32 v103, v103, v102
	v_fma_f32 v103, v103, v102, v102
	v_mul_f32_e32 v103, 0x3f4c422a, v103
	v_add_f32_e64 v104, |v103|, |v103|
	v_mul_f32_e32 v104, 0x3fb8aa3b, v104
	v_exp_f32_e32 v104, v104
	s_nop 0
	v_add_f32_e32 v104, 1.0, v104
	v_rcp_f32_e32 v104, v104
	s_nop 0
	v_fma_f32 v104, v104, -2.0, 1.0
	v_and_b32_e32 v91, 0xffff0000, v91
	v_mul_f32_e32 v105, 0x3d372713, v91
	v_mul_f32_e32 v105, v105, v91
	v_fma_f32 v105, v105, v91, v91
	v_mul_f32_e32 v105, 0x3f4c422a, v105
	v_add_f32_e64 v106, |v105|, |v105|
	v_mul_f32_e32 v106, 0x3fb8aa3b, v106
	v_exp_f32_e32 v106, v106
	s_nop 0
	v_add_f32_e32 v106, 1.0, v106
	v_rcp_f32_e32 v106, v106
	s_nop 0
	v_fma_f32 v106, v106, -2.0, 1.0
	v_bfi_b32 v103, s30, v104, v103
	v_mul_f32_e32 v102, 0.5, v102
	v_add_f32_e32 v103, 1.0, v103
	v_mul_f32_e32 v102, v102, v103
	v_add_f32_e32 v88, v88, v98
	v_mul_f32_e32 v102, v88, v102
	v_mul_f32_e32 v88, 0.5, v92
	v_bfi_b32 v92, s30, v96, v93
	v_add_f32_e32 v92, 1.0, v92
	v_mul_f32_e32 v88, v88, v92
	v_add_f32_e32 v86, v86, v98
	v_bfi_b32 v99, s30, v99, v97
	v_mov_b32_e32 v132, v87
	v_mul_f32_e32 v88, v86, v88
	v_mul_f32_e32 v90, 0.5, v90
	v_pk_add_f32 v[86:87], v[132:133], v[98:99]
	v_bfi_b32 v99, s30, v106, v105
	v_mul_f32_e32 v87, v90, v87
	v_mul_f32_e32 v86, v86, v87
	v_mov_b32_e32 v132, v89
	v_cvt_pk_bf16_f32 v86, v88, v86
	v_mul_f32_e32 v87, 0.5, v91
	v_pk_add_f32 v[88:89], v[132:133], v[98:99]
	s_nop 0
	v_mul_f32_e32 v87, v87, v89
	v_mul_f32_e32 v87, v88, v87
	v_cvt_pk_bf16_f32 v87, v102, v87
	global_store_dwordx2 v[94:95], v[86:87], off offset:2112
	v_mov_b64_e32 v[86:87], v[180:181]
	v_lshlrev_b32_e32 v88, 16, v86
	v_mul_f32_e32 v89, 0x3d372713, v88
	v_mul_f32_e32 v89, v89, v88
	v_fma_f32 v89, v89, v88, v88
	v_mul_f32_e32 v89, 0x3f4c422a, v89
	v_add_f32_e64 v90, |v89|, |v89|
	v_mul_f32_e32 v90, 0x3fb8aa3b, v90
	v_exp_f32_e32 v90, v90
	s_nop 0
	v_add_f32_e32 v90, 1.0, v90
	v_rcp_f32_e32 v90, v90
	s_nop 0
	v_fma_f32 v90, v90, -2.0, 1.0
	v_and_b32_e32 v86, 0xffff0000, v86
	v_mul_f32_e32 v91, 0x3d372713, v86
	v_mul_f32_e32 v91, v91, v86
	v_fma_f32 v91, v91, v86, v86
	v_mul_f32_e32 v91, 0x3f4c422a, v91
	v_add_f32_e64 v92, |v91|, |v91|
	v_mul_f32_e32 v92, 0x3fb8aa3b, v92
	v_exp_f32_e32 v92, v92
	s_nop 0
	v_add_f32_e32 v92, 1.0, v92
	v_rcp_f32_e32 v92, v92
	s_nop 0
	v_fma_f32 v92, v92, -2.0, 1.0
	v_lshlrev_b32_e32 v93, 16, v87
	v_mul_f32_e32 v96, 0x3d372713, v93
	v_mul_f32_e32 v96, v96, v93
	v_fma_f32 v96, v96, v93, v93
	v_mul_f32_e32 v96, 0x3f4c422a, v96
	v_add_f32_e64 v97, |v96|, |v96|
	v_mul_f32_e32 v97, 0x3fb8aa3b, v97
	v_exp_f32_e32 v97, v97
	s_nop 0
	v_add_f32_e32 v97, 1.0, v97
	v_rcp_f32_e32 v97, v97
	s_nop 0
	v_fma_f32 v97, v97, -2.0, 1.0
	v_and_b32_e32 v87, 0xffff0000, v87
	v_mul_f32_e32 v99, 0x3d372713, v87
	v_mul_f32_e32 v99, v99, v87
	v_fma_f32 v99, v99, v87, v87
	v_mul_f32_e32 v100, 0x3f4c422a, v99
	v_cmp_nlt_f32_e64 s[2:3], |v100|, s26
	s_and_saveexec_b64 s[18:19], s[2:3]
	s_xor_b64 s[18:19], exec, s[18:19]
	s_cbranch_execz .LBB0_3450
	v_add_f32_e64 v99, |v100|, |v100|
	v_mul_f32_e32 v101, 0x3fb8aa3b, v99
	v_rndne_f32_e32 v102, v101
	v_sub_f32_e32 v103, v101, v102
	v_fma_f32 v101, v99, s27, -v101
	v_fmac_f32_e32 v101, 0x32a5705f, v99
	v_add_f32_e32 v101, v103, v101
	v_cvt_i32_f32_e32 v102, v102
	v_exp_f32_e32 v101, v101
	v_cmp_ngt_f32_e32 vcc, s28, v99
	v_ldexp_f32 v101, v101, v102
	s_nop 0
	v_cndmask_b32_e32 v101, 0, v101, vcc
	v_cmp_nlt_f32_e32 vcc, s29, v99
	s_nop 1
	v_cndmask_b32_e32 v99, v158, v101, vcc
	v_add_f32_e32 v99, 1.0, v99
	v_rcp_f32_e32 v99, v99
	s_nop 0
	v_fma_f32 v101, v99, -2.0, 1.0
